# baseline (speedup 1.0000x reference)
_Z8k1_fusedPKfS0_S0_S0_S0_PDF16_PfPiPDv8_DF16_:
	s_load_dwordx4 s[4:7], s[0:1], 0x0
	s_load_dwordx2 s[8:9], s[0:1], 0x10
	s_load_dwordx2 s[12:13], s[0:1], 0x20
	s_cmp_eq_u32 s2, 0
	s_cselect_b64 s[10:11], -1, 0
	v_cmp_gt_u32_e32 vcc, 16, v0
	s_and_b64 s[16:17], s[10:11], vcc
	s_and_saveexec_b64 s[14:15], s[16:17]
	s_cbranch_execz .LBB0_2
	s_load_dwordx2 s[16:17], s[0:1], 0x38
	v_mov_b32_e32 v1, 0
	s_waitcnt lgkmcnt(0)
	v_lshl_add_u64 v[2:3], v[0:1], 2, s[16:17]
	global_store_dword v[2:3], v1, off sc0 sc1
.LBB0_2:
	s_or_b64 exec, exec, s[14:15]
	s_load_dwordx2 s[14:15], s[0:1], 0x18
	s_movk_i32 s3, 0xa0
	v_cmp_gt_u32_e32 vcc, s3, v0
	s_and_b64 s[18:19], s[10:11], vcc
	s_and_saveexec_b64 s[16:17], s[18:19]
	s_cbranch_execz .LBB0_4
	s_load_dwordx2 s[18:19], s[0:1], 0x30
	v_mov_b32_e32 v1, 0
	v_mov_b32_e32 v4, v1
	v_mov_b32_e32 v5, v1
	s_waitcnt lgkmcnt(0)
	v_lshl_add_u64 v[2:3], v[0:1], 3, s[18:19]
	global_store_dwordx2 v[2:3], v[4:5], off sc0 sc1
.LBB0_4:
	s_or_b64 exec, exec, s[16:17]
	v_bfe_u32 v68, v0, 4, 5
	v_mul_u32_u24_e32 v2, 0x120, v68
	v_and_b32_e32 v1, 15, v0
	v_lshlrev_b32_e32 v2, 2, v2
	v_mov_b32_e32 v3, 0
	s_waitcnt lgkmcnt(0)
	v_lshl_add_u64 v[4:5], s[14:15], 0, v[2:3]
	v_lshlrev_b32_e32 v2, 3, v1
	v_lshl_add_u64 v[4:5], v[4:5], 0, v[2:3]
	global_load_dwordx2 v[64:65], v[4:5], off
	global_load_dwordx2 v[62:63], v[4:5], off offset:128
	global_load_dwordx2 v[60:61], v[4:5], off offset:256
	global_load_dwordx2 v[58:59], v[4:5], off offset:384
	global_load_dwordx2 v[56:57], v[4:5], off offset:512
	global_load_dwordx2 v[54:55], v[4:5], off offset:640
	global_load_dwordx2 v[52:53], v[4:5], off offset:768
	global_load_dwordx2 v[50:51], v[4:5], off offset:896
	global_load_dwordx2 v[48:49], v[4:5], off offset:1024
	v_min_u32_e32 v69, 0xd7, v0
	v_lshlrev_b32_e32 v2, 4, v69
	global_load_dwordx4 v[4:7], v2, s[6:7]
	v_mov_b32_e32 v2, s13
	v_mov_b32_e32 v8, s9
	v_cmp_gt_u32_e32 vcc, 8, v1
	v_lshlrev_b32_e32 v19, 4, v0
	s_movk_i32 s3, 0x17f
	v_cndmask_b32_e32 v9, v2, v8, vcc
	v_mov_b32_e32 v2, s12
	v_mov_b32_e32 v8, s8
	v_cndmask_b32_e32 v8, v2, v8, vcc
	v_and_b32_e32 v2, 0x70, v19
	v_lshl_add_u64 v[8:9], v[8:9], 0, v[2:3]
	global_load_dwordx4 v[8:11], v[8:9], off
	v_cmp_lt_u32_e64 s[8:9], s3, v0
	v_mov_b32_e32 v12, 0xfffffe80
	s_lshl_b32 s3, s2, 1
	v_cndmask_b32_e64 v2, 0, 1, s[8:9]
	v_cndmask_b32_e64 v12, 0, v12, s[8:9]
	s_ashr_i32 s20, s2, 4
	v_and_or_b32 v137, s3, 2, v2
	s_lshl_b32 s2, s2, 3
	v_add_u32_e32 v142, v12, v0
	v_and_b32_e32 v15, 63, v0
	v_and_b32_e32 v134, 31, v0
	v_bfe_u32 v138, v0, 5, 1
	s_and_b32 s21, s2, 0x70
	v_lshlrev_b32_e32 v143, 5, v137
	v_lshlrev_b32_e32 v70, 2, v69
	s_mov_b32 s25, 0xe38f
	v_mul_u32_u24_sdwa v2, v142, s25 dst_sel:DWORD dst_unused:UNUSED_PAD src0_sel:WORD_0 src1_sel:DWORD
	v_lshrrev_b32_e32 v2, 21, v2
	s_add_i32 s2, s21, -3
	v_add_u32_e32 v14, -3, v143
	v_mul_i32_i24_e32 v12, 0xffffffdc, v2
	v_add_u32_e32 v2, s2, v2
	v_add3_u32 v31, v14, v142, v12
	s_lshl_b32 s3, s20, 14
	v_max_i32_e32 v13, 0, v2
	v_mov_b32_e32 v20, 0x7f
	v_add_u32_e32 v35, 1, v31
	v_lshl_or_b32 v18, v13, 7, s3
	v_med3_i32 v12, v31, 0, v20
	v_med3_i32 v16, v35, 0, v20
	v_or_b32_e32 v12, v12, v18
	v_or_b32_e32 v16, v16, v18
	v_lshl_add_u32 v12, v12, 1, v12
	v_lshl_add_u32 v16, v16, 1, v16
	v_ashrrev_i32_e32 v13, 31, v12
	v_ashrrev_i32_e32 v17, 31, v16
	v_lshl_add_u64 v[12:13], v[12:13], 2, s[4:5]
	v_lshl_add_u64 v[16:17], v[16:17], 2, s[4:5]
	v_add_u32_e32 v27, 0x180, v142
	global_load_dwordx3 v[40:42], v[12:13], off
	global_load_dwordx3 v[32:34], v[16:17], off
	v_add_u32_e32 v39, 2, v31
	v_min_u32_e32 v16, 0x317, v27
	s_movk_i32 s23, 0xffdc
	v_med3_i32 v12, v39, 0, v20
	v_mul_u32_u24_e32 v17, 0x71d, v16
	v_or_b32_e32 v12, v12, v18
	v_mul_i32_i24_sdwa v18, v17, s23 dst_sel:DWORD dst_unused:UNUSED_PAD src0_sel:WORD_1 src1_sel:DWORD
	v_add_u32_sdwa v43, s2, v17 dst_sel:DWORD dst_unused:UNUSED_PAD src0_sel:DWORD src1_sel:WORD_1
	v_min_u32_e32 v17, 0x7f, v43
	v_add3_u32 v47, v14, v16, v18
	v_lshl_or_b32 v18, v17, 7, s3
	v_med3_i32 v16, v47, 0, v20
	v_lshl_add_u32 v12, v12, 1, v12
	v_or_b32_e32 v16, v16, v18
	v_ashrrev_i32_e32 v13, 31, v12
	v_lshl_add_u32 v16, v16, 1, v16
	v_lshl_add_u64 v[12:13], v[12:13], 2, s[4:5]
	v_ashrrev_i32_e32 v17, 31, v16
	v_add_u32_e32 v122, 1, v47
	v_lshl_add_u64 v[16:17], v[16:17], 2, s[4:5]
	global_load_dwordx3 v[44:46], v[12:13], off
	global_load_dwordx3 v[24:26], v[16:17], off
	v_med3_i32 v12, v122, 0, v20
	v_add_u32_e32 v123, 2, v47
	v_or_b32_e32 v12, v12, v18
	v_med3_i32 v16, v123, 0, v20
	v_lshl_add_u32 v12, v12, 1, v12
	v_or_b32_e32 v16, v16, v18
	v_ashrrev_i32_e32 v13, 31, v12
	v_lshl_add_u32 v16, v16, 1, v16
	v_lshl_add_u64 v[12:13], v[12:13], 2, s[4:5]
	v_ashrrev_i32_e32 v17, 31, v16
	v_add_u32_e32 v23, 0x300, v142
	v_lshl_add_u64 v[16:17], v[16:17], 2, s[4:5]
	global_load_dwordx3 v[36:38], v[12:13], off
	global_load_dwordx3 v[20:22], v[16:17], off
	v_min_u32_e32 v12, 0x317, v23
	v_mul_u32_u24_e32 v13, 0x71d, v12
	v_mul_i32_i24_sdwa v16, v13, s23 dst_sel:DWORD dst_unused:UNUSED_PAD src0_sel:WORD_1 src1_sel:DWORD
	v_add_u32_sdwa v124, s2, v13 dst_sel:DWORD dst_unused:UNUSED_PAD src0_sel:DWORD src1_sel:WORD_1
	v_min_u32_e32 v13, 0x7f, v124
	v_add3_u32 v125, v14, v12, v16
	v_lshl_or_b32 v14, v13, 7, s3
	v_min_u32_e32 v12, 0x7f, v125
	v_add_u32_e32 v126, 1, v125
	v_or_b32_e32 v12, v12, v14
	v_min_u32_e32 v16, 0x7f, v126
	v_lshl_add_u32 v12, v12, 1, v12
	v_or_b32_e32 v16, v16, v14
	v_ashrrev_i32_e32 v13, 31, v12
	v_lshl_add_u32 v16, v16, 1, v16
	v_lshl_add_u64 v[12:13], v[12:13], 2, s[4:5]
	v_ashrrev_i32_e32 v17, 31, v16
	v_add_u32_e32 v127, 2, v125
	v_lshl_add_u64 v[66:67], v[16:17], 2, s[4:5]
	global_load_dwordx3 v[28:30], v[12:13], off
	global_load_dwordx3 v[16:18], v[66:67], off
	v_min_u32_e32 v12, 0x7f, v127
	v_or_b32_e32 v12, v12, v14
	v_lshl_add_u32 v12, v12, 1, v12
	v_ashrrev_i32_e32 v13, 31, v12
	v_lshl_add_u64 v[12:13], v[12:13], 2, s[4:5]
	global_load_dwordx3 v[12:14], v[12:13], off
	s_mov_b32 s24, 0xffff
	v_lshlrev_b32_e32 v66, 1, v0
	v_and_b32_e32 v67, 4, v0
	v_and_or_b32 v66, v66, 2, v67
	v_bfe_u32 v67, v0, 3, 1
	v_and_or_b32 v67, v0, 2, v67
	v_lshlrev_b32_e32 v68, 4, v68
	s_movk_i32 s2, 0x210
	v_mad_u32_u24 v67, v67, s2, v68
	v_lshl_or_b32 v66, v66, 1, v67
	s_waitcnt vmcnt(11)
	v_cvt_pk_f16_f32 v48, v48, v49
	v_mul_lo_u16_e32 v49, 57, v69
	ds_write_b32 v66, v48 offset:42496
	v_lshrrev_b32_e32 v48, 3, v69
	v_lshrrev_b16_e32 v49, 12, v49
	v_cvt_pk_f16_f32 v50, v50, v51
	v_mad_i32_i24 v48, v49, -9, v48
	ds_write_b32 v66, v50 offset:40384
	v_lshlrev_b32_e32 v50, 2, v48
	v_and_b32_e32 v50, 0xfffffe0, v50
	v_lshl_add_u32 v49, v49, 6, v50
	v_and_b32_e32 v48, 7, v48
	s_waitcnt vmcnt(10)
	v_cvt_f16_f32_e32 v4, v4
	v_and_or_b32 v49, v70, 28, v49
	v_lshlrev_b32_e32 v48, 1, v48
	v_cvt_f16_f32_e32 v5, v5
	v_lshl_or_b32 v48, v49, 4, v48
	v_cvt_f16_f32_e32 v6, v6
	v_cvt_pk_f16_f32 v64, v64, v65
	v_cvt_pk_f16_f32 v62, v62, v63
	v_cvt_pk_f16_f32 v60, v60, v61
	v_cvt_pk_f16_f32 v58, v58, v59
	v_cvt_pk_f16_f32 v56, v56, v57
	v_cvt_pk_f16_f32 v54, v54, v55
	v_cvt_pk_f16_f32 v52, v52, v53
	v_add_u32_e32 v48, 0x23000, v48
	v_cvt_f16_f32_e32 v7, v7
	ds_write_b32 v66, v64 offset:25600
	ds_write_b32 v66, v62 offset:27712
	ds_write_b32 v66, v60 offset:29824
	ds_write_b32 v66, v58 offset:31936
	ds_write_b32 v66, v56 offset:34048
	ds_write_b32 v66, v54 offset:36160
	ds_write_b32 v66, v52 offset:38272
	ds_write_b16 v48, v4
	ds_write_b16 v48, v5 offset:16
	ds_write_b16 v48, v6 offset:32
	ds_write_b16 v48, v7 offset:48
	v_mov_b32_e32 v4, 0x23c00
	v_lshl_or_b32 v1, v1, 4, v4
	s_waitcnt vmcnt(9)
	ds_write_b128 v1, v[8:11]
	v_lshlrev_b32_e32 v139, 4, v134
	v_mad_u32_u24 v1, v138, s2, v139
	s_waitcnt lgkmcnt(0)
	s_barrier
	ds_read_b128 v[50:53], v1 offset:26656
	ds_read_b128 v[54:57], v1 offset:27712
	ds_read_b128 v[58:61], v1 offset:28768
	ds_read_b128 v[62:65], v1 offset:29824
	ds_read_b128 v[66:69], v1 offset:30880
	ds_read_b128 v[70:73], v1 offset:31936
	ds_read_b128 v[74:77], v1 offset:32992
	ds_read_b128 v[78:81], v1 offset:34048
	ds_read_b128 v[82:85], v1 offset:35104
	ds_read_b128 v[86:89], v1 offset:36160
	ds_read_b128 v[90:93], v1 offset:37216
	ds_read_b128 v[94:97], v1 offset:38272
	ds_read_b128 v[98:101], v1 offset:39328
	ds_read_b128 v[102:105], v1 offset:40384
	ds_read_b128 v[106:109], v1 offset:41440
	ds_read_b128 v[110:113], v1 offset:42496
	ds_read_b128 v[114:117], v1 offset:25600
	ds_read_b128 v[118:121], v1 offset:43552
	v_cmp_gt_u32_e32 vcc, 64, v0
	s_and_b64 s[4:5], s[10:11], vcc
	s_and_saveexec_b64 s[2:3], s[4:5]
	s_cbranch_execz .LBB0_6
	s_load_dwordx2 s[4:5], s[0:1], 0x40
	v_mov_b32_e32 v1, v3
	s_waitcnt lgkmcnt(0)
	v_lshl_add_u64 v[4:5], v[0:1], 4, s[4:5]
	v_add_co_u32_e32 v6, vcc, 0x1000, v4
	global_store_dwordx4 v[4:5], v[114:117], off sc0 sc1
	global_store_dwordx4 v[4:5], v[50:53], off offset:1024 sc0 sc1
	global_store_dwordx4 v[4:5], v[54:57], off offset:2048 sc0 sc1
	global_store_dwordx4 v[4:5], v[58:61], off offset:3072 sc0 sc1
	v_addc_co_u32_e32 v7, vcc, 0, v5, vcc
	global_store_dwordx4 v[6:7], v[62:65], off sc0 sc1
	global_store_dwordx4 v[6:7], v[66:69], off offset:1024 sc0 sc1
	global_store_dwordx4 v[6:7], v[70:73], off offset:2048 sc0 sc1
	global_store_dwordx4 v[6:7], v[74:77], off offset:3072 sc0 sc1
	v_add_co_u32_e32 v6, vcc, 0x2000, v4
	s_nop 1
	v_addc_co_u32_e32 v7, vcc, 0, v5, vcc
	global_store_dwordx4 v[6:7], v[78:81], off sc0 sc1
	global_store_dwordx4 v[6:7], v[82:85], off offset:1024 sc0 sc1
	global_store_dwordx4 v[6:7], v[86:89], off offset:2048 sc0 sc1
	global_store_dwordx4 v[6:7], v[90:93], off offset:3072 sc0 sc1
	v_add_co_u32_e32 v6, vcc, 0x3000, v4
	s_nop 1
	v_addc_co_u32_e32 v7, vcc, 0, v5, vcc
	v_add_co_u32_e32 v4, vcc, 0x4000, v4
	global_store_dwordx4 v[6:7], v[94:97], off sc0 sc1
	global_store_dwordx4 v[6:7], v[98:101], off offset:1024 sc0 sc1
	global_store_dwordx4 v[6:7], v[102:105], off offset:2048 sc0 sc1
	global_store_dwordx4 v[6:7], v[106:109], off offset:3072 sc0 sc1
	v_addc_co_u32_e32 v5, vcc, 0, v5, vcc
	global_store_dwordx4 v[4:5], v[110:113], off sc0 sc1
	global_store_dwordx4 v[4:5], v[118:121], off offset:1024 sc0 sc1
